# unit-boundary trimming: G1/G2 accumulator clears as 64-bit moves (124 instead of 248 instructions per unit start)
# speedup vs baseline: 1.0101x; 1.0101x over previous
.LBB0_309:
	s_ashr_i32 s19, s18, 31
	s_lshl_b64 s[20:21], s[18:19], 19
	v_readlane_b32 s22, v242, 53
	v_readlane_b32 s23, v242, 54
	s_add_u32 s20, s22, s20
	s_addc_u32 s21, s23, s21
	s_and_b64 s[22:23], s[6:7], exec
	s_cselect_b32 s19, s21, s25
	s_cselect_b32 s33, s20, s24
	s_ashr_i32 s17, s16, 31
	s_lshl_b64 s[22:23], s[16:17], 19
	s_add_u32 s22, s30, s22
	s_addc_u32 s23, s31, s23
	s_and_b64 s[28:29], s[6:7], exec
	s_cselect_b32 s17, s23, s27
	s_cselect_b32 s53, s22, s26
	s_add_u32 s24, s24, 0x40080
	s_addc_u32 s25, s25, 0
	s_add_u32 s54, s26, 0x100
	s_addc_u32 s55, s27, 0
	s_mov_b32 s56, -2
	v_mov_b64_e32 v[0:1], 0
	v_mov_b64_e32 v[2:3], 0
	v_mov_b64_e32 v[4:5], 0
	v_mov_b64_e32 v[6:7], 0
	v_mov_b64_e32 v[8:9], 0
	v_mov_b64_e32 v[10:11], 0
	v_mov_b64_e32 v[12:13], 0
	v_mov_b64_e32 v[14:15], 0
	v_mov_b64_e32 v[16:17], 0
	v_mov_b64_e32 v[18:19], 0
	v_mov_b64_e32 v[20:21], 0
	v_mov_b64_e32 v[22:23], 0
	v_mov_b64_e32 v[24:25], 0
	v_mov_b64_e32 v[26:27], 0
	v_mov_b64_e32 v[28:29], 0
	v_mov_b64_e32 v[30:31], 0
	v_mov_b64_e32 v[32:33], 0
	v_mov_b64_e32 v[34:35], 0
	v_mov_b64_e32 v[36:37], 0
	v_mov_b64_e32 v[38:39], 0
	v_mov_b64_e32 v[40:41], 0
	v_mov_b64_e32 v[42:43], 0
	v_mov_b64_e32 v[44:45], 0
	v_mov_b64_e32 v[46:47], 0
	v_mov_b64_e32 v[48:49], 0
	v_mov_b64_e32 v[50:51], 0
	v_mov_b64_e32 v[52:53], 0
	v_mov_b64_e32 v[54:55], 0
	v_mov_b64_e32 v[56:57], 0
	v_mov_b64_e32 v[58:59], 0
	v_mov_b64_e32 v[60:61], 0
	v_mov_b64_e32 v[62:63], 0
	v_mov_b64_e32 v[66:67], 0
	v_mov_b64_e32 v[68:69], 0
	v_mov_b64_e32 v[70:71], 0
	v_mov_b64_e32 v[72:73], 0
	v_mov_b64_e32 v[74:75], 0
	v_mov_b64_e32 v[76:77], 0
	v_mov_b64_e32 v[78:79], 0
	v_mov_b64_e32 v[80:81], 0
	v_mov_b64_e32 v[82:83], 0
	v_mov_b64_e32 v[84:85], 0
	v_mov_b64_e32 v[86:87], 0
	v_mov_b64_e32 v[88:89], 0
	v_mov_b64_e32 v[90:91], 0
	v_mov_b64_e32 v[92:93], 0
	v_mov_b64_e32 v[94:95], 0
	v_mov_b64_e32 v[96:97], 0
	v_mov_b64_e32 v[98:99], 0
	v_mov_b64_e32 v[100:101], 0
	v_mov_b64_e32 v[102:103], 0
	v_mov_b64_e32 v[104:105], 0
	v_mov_b64_e32 v[106:107], 0
	v_mov_b64_e32 v[108:109], 0
	v_mov_b64_e32 v[110:111], 0
	v_mov_b64_e32 v[112:113], 0
	v_mov_b64_e32 v[114:115], 0
	v_mov_b64_e32 v[116:117], 0
	v_mov_b64_e32 v[118:119], 0
	v_mov_b64_e32 v[120:121], 0
	v_mov_b64_e32 v[122:123], 0
	v_mov_b64_e32 v[124:125], 0
	v_mov_b64_e32 v[126:127], 0
	v_mov_b64_e32 v[128:129], 0

.LBB0_813:
	s_add_i32 s51, s51, 1
	s_mov_b64 s[0:1], s[14:15]
	s_mov_b32 s14, s10
	s_mov_b32 s53, s10
	s_mul_i32 s10, s51, s73
	s_add_i32 s10, s10, s71
	s_cmp_lt_i32 s10, s2
	s_mov_b32 s15, s52
	s_mov_b32 s54, s52
	s_cselect_b64 s[24:25], -1, 0
	s_ashr_i32 s26, s10, 2
	s_and_b32 s52, s10, 3
	s_cmp_gt_i32 s26, 63
	s_mov_b64 s[4:5], s[12:13]
	s_cselect_b64 s[12:13], -1, 0
	s_cmp_lg_u64 s[12:13], 0
	v_readlane_b32 s12, v241, 10
	s_addc_u32 s10, s26, 1
	v_readlane_b32 s13, v241, 11
	s_and_b64 s[12:13], s[12:13], exec
	s_cselect_b32 s10, s10, s26
	s_and_b64 s[12:13], s[24:25], exec
	s_cselect_b32 s14, s10, s14
	s_cselect_b32 s12, s52, s15
	s_ashr_i32 s15, s14, 31
	s_lshl_b64 s[14:15], s[14:15], 19
	s_add_u32 s14, s3, s14
	s_addc_u32 s15, s28, s15
	s_and_b64 s[26:27], s[24:25], exec
	s_cselect_b32 s55, s15, s1
	s_cselect_b32 s56, s14, s0
	s_ashr_i32 s13, s12, 31
	s_lshl_b64 s[12:13], s[12:13], 19
	s_add_u32 s12, s29, s12
	s_addc_u32 s13, s30, s13
	s_and_b64 s[26:27], s[24:25], exec
	s_cselect_b32 s57, s13, s5
	s_cselect_b32 s58, s12, s4
	s_add_u32 s0, s0, 0x40080
	s_addc_u32 s1, s1, 0
	s_add_u32 s59, s4, 0x100
	s_addc_u32 s60, s5, 0
	s_mov_b32 s61, -2
	v_mov_b64_e32 v[0:1], 0
	v_mov_b64_e32 v[2:3], 0
	v_mov_b64_e32 v[4:5], 0
	v_mov_b64_e32 v[6:7], 0
	v_mov_b64_e32 v[8:9], 0
	v_mov_b64_e32 v[10:11], 0
	v_mov_b64_e32 v[12:13], 0
	v_mov_b64_e32 v[14:15], 0
	v_mov_b64_e32 v[16:17], 0
	v_mov_b64_e32 v[18:19], 0
	v_mov_b64_e32 v[20:21], 0
	v_mov_b64_e32 v[22:23], 0
	v_mov_b64_e32 v[24:25], 0
	v_mov_b64_e32 v[26:27], 0
	v_mov_b64_e32 v[28:29], 0
	v_mov_b64_e32 v[30:31], 0
	v_mov_b64_e32 v[32:33], 0
	v_mov_b64_e32 v[34:35], 0
	v_mov_b64_e32 v[36:37], 0
	v_mov_b64_e32 v[38:39], 0
	v_mov_b64_e32 v[40:41], 0
	v_mov_b64_e32 v[42:43], 0
	v_mov_b64_e32 v[44:45], 0
	v_mov_b64_e32 v[46:47], 0
	v_mov_b64_e32 v[48:49], 0
	v_mov_b64_e32 v[50:51], 0
	v_mov_b64_e32 v[52:53], 0
	v_mov_b64_e32 v[54:55], 0
	v_mov_b64_e32 v[56:57], 0
	v_mov_b64_e32 v[58:59], 0
	v_mov_b64_e32 v[60:61], 0
	v_mov_b64_e32 v[62:63], 0
	v_mov_b64_e32 v[82:83], 0
	v_mov_b64_e32 v[84:85], 0
	v_mov_b64_e32 v[86:87], 0
	v_mov_b64_e32 v[88:89], 0
	v_mov_b64_e32 v[90:91], 0
	v_mov_b64_e32 v[92:93], 0
	v_mov_b64_e32 v[94:95], 0
	v_mov_b64_e32 v[96:97], 0
	v_mov_b64_e32 v[98:99], 0
	v_mov_b64_e32 v[100:101], 0
	v_mov_b64_e32 v[102:103], 0
	v_mov_b64_e32 v[104:105], 0
	v_mov_b64_e32 v[106:107], 0
	v_mov_b64_e32 v[108:109], 0
	v_mov_b64_e32 v[110:111], 0
	v_mov_b64_e32 v[112:113], 0
	v_mov_b64_e32 v[114:115], 0
	v_mov_b64_e32 v[116:117], 0
	v_mov_b64_e32 v[118:119], 0
	v_mov_b64_e32 v[120:121], 0
	v_mov_b64_e32 v[122:123], 0
	v_mov_b64_e32 v[124:125], 0
	v_mov_b64_e32 v[126:127], 0
	v_mov_b64_e32 v[128:129], 0
	v_mov_b64_e32 v[130:131], 0
	v_mov_b64_e32 v[132:133], 0
	v_mov_b64_e32 v[134:135], 0
	v_mov_b64_e32 v[136:137], 0
	v_mov_b32_e32 v138, v0
	v_mov_b32_e32 v139, v0
	v_mov_b32_e32 v140, v0
	v_mov_b32_e32 v141, v0
	v_mov_b32_e32 v142, v0
	v_mov_b32_e32 v143, v0
	v_mov_b32_e32 v144, v0
	v_mov_b32_e32 v145, v0
